# speedup vs baseline: 1.0180x; 1.0064x over previous
.LBB1_1:
	s_waitcnt lgkmcnt(0)
	v_mfma_f32_32x32x16_f16 v[114:129], v[198:201], v[186:189], v[114:129]
	s_mov_b32 s44, s33
	s_mov_b32 s33, s43
	v_mfma_f32_32x32x16_f16 v[98:113], v[198:201], v[182:185], v[98:113]
	v_add_u32_e32 v219, s33, v215
	ds_read_b128 v[198:201], v219 offset:8192
	ds_read_b128 v[220:223], v219 offset:10240
	ds_read_b128 v[224:227], v219 offset:12288
	ds_read_b128 v[228:231], v219 offset:14336
	v_add_u32_e32 v219, s33, v214
	ds_read_b128 v[232:235], v219
	ds_read_b128 v[236:239], v219 offset:2048
	s_waitcnt vmcnt(10)
	v_cvt_pk_f16_f32 v162, v162, v163
	v_cvt_pk_f16_f32 v163, v164, v165
	v_cvt_pk_f16_f32 v164, v154, v155
	v_cvt_pk_f16_f32 v165, v156, v157
	v_add_u32_e32 v154, s34, v209
	ds_write_b64 v154, v[162:163]
	v_add_u32_e32 v154, s34, v248
	ds_write_b64 v154, v[164:165]
	v_mfma_f32_32x32x16_f16 v[82:97], v[194:197], v[186:189], v[82:97]
	v_add_u32_e32 v154, s34, v208
	s_waitcnt vmcnt(9)
	ds_write_b128 v154, v[158:161] offset:8192
	s_waitcnt vmcnt(8)
	ds_write_b128 v154, v[174:177] offset:16384
	v_mfma_f32_32x32x16_f16 v[66:81], v[194:197], v[182:185], v[66:81]
	v_mfma_f32_32x32x16_f16 v[50:65], v[190:193], v[186:189], v[50:65]
	s_waitcnt vmcnt(7)
	ds_write_b128 v154, v[166:169] offset:24576
	s_waitcnt vmcnt(6)
	ds_write_b128 v154, v[170:173] offset:32768
	v_mfma_f32_32x32x16_f16 v[34:49], v[190:193], v[182:185], v[34:49]
	v_add_co_u32_e64 v158, s[0:1], s36, v202
	global_load_dwordx4 v[154:157], v[252:253], off offset:-144 sc1 nt
	global_load_dwordx4 v[162:165], v[204:205], off offset:-144 sc1 nt
	v_addc_co_u32_e64 v159, s[0:1], -1, v203, s[0:1]
	v_add_co_u32_e64 v166, s[0:1], s37, v202
	v_mfma_f32_32x32x16_f16 v[18:33], v[178:181], v[186:189], v[18:33]
	s_nop 0
	v_addc_co_u32_e64 v167, s[0:1], -1, v203, s[0:1]
	global_load_dwordx4 v[158:161], v[158:159], off sc1
	s_nop 0
	global_load_dwordx4 v[174:177], v[166:167], off sc1
	v_add_co_u32_e64 v166, s[0:1], s38, v202
	s_nop 1
	v_addc_co_u32_e64 v167, s[0:1], -1, v203, s[0:1]
	v_add_co_u32_e64 v170, s[0:1], s39, v202
	v_mfma_f32_32x32x16_f16 v[2:17], v[178:181], v[182:185], v[2:17]
	s_nop 0
	v_addc_co_u32_e64 v171, s[0:1], -1, v203, s[0:1]
	global_load_dwordx4 v[166:169], v[166:167], off sc1
	s_nop 0
	global_load_dwordx4 v[170:173], v[170:171], off sc1
	v_add_u32_e32 v190, s44, v216
	ds_read_b128 v[178:181], v190 offset:8192
	ds_read_b128 v[182:185], v190 offset:10240
	ds_read_b128 v[186:189], v190 offset:12288
	ds_read_b128 v[190:193], v190 offset:14336
	v_add_u32_e32 v219, s44, v217
	ds_read_b128 v[194:197], v219
	ds_read_b128 v[240:243], v219 offset:2048
	s_waitcnt lgkmcnt(12)
	v_mfma_f32_32x32x16_f16 v[114:129], v[198:201], v[232:235], v[114:129]
	s_waitcnt lgkmcnt(11)
	v_mfma_f32_32x32x16_f16 v[98:113], v[198:201], v[236:239], v[98:113]
	v_mfma_f32_32x32x16_f16 v[82:97], v[220:223], v[232:235], v[82:97]
	v_mfma_f32_32x32x16_f16 v[66:81], v[220:223], v[236:239], v[66:81]
	v_mfma_f32_32x32x16_f16 v[50:65], v[224:227], v[232:235], v[50:65]
	v_mfma_f32_32x32x16_f16 v[34:49], v[224:227], v[236:239], v[34:49]
	v_mfma_f32_32x32x16_f16 v[18:33], v[228:231], v[232:235], v[18:33]
	v_mfma_f32_32x32x16_f16 v[2:17], v[228:231], v[236:239], v[2:17]
	s_waitcnt lgkmcnt(1)
	v_mfma_f32_32x32x16_f16 v[114:129], v[178:181], v[194:197], v[114:129]
	s_waitcnt lgkmcnt(0)
	s_barrier
	s_waitcnt lgkmcnt(0)
	v_mfma_f32_32x32x16_f16 v[98:113], v[178:181], v[240:243], v[98:113]
	v_add_u32_e32 v178, s44, v215
	ds_read_b128 v[220:223], v178 offset:8192
	ds_read_b128 v[224:227], v178 offset:10240
	ds_read_b128 v[228:231], v178 offset:12288
	ds_read_b128 v[232:235], v178 offset:14336
	v_add_u32_e32 v178, s44, v214
	ds_read_b128 v[236:239], v178
	ds_read_b128 v[244:247], v178 offset:2048
	s_waitcnt vmcnt(10)
	v_cvt_pk_f16_f32 v150, v150, v151
	v_cvt_pk_f16_f32 v151, v152, v153
	v_cvt_pk_f16_f32 v152, v142, v143
	v_cvt_pk_f16_f32 v153, v144, v145
	v_add_u32_e32 v142, s33, v209
	ds_write_b64 v142, v[150:151]
	v_add_u32_e32 v142, s33, v248
	ds_write_b64 v142, v[152:153]
	v_mfma_f32_32x32x16_f16 v[82:97], v[182:185], v[194:197], v[82:97]
	v_add_u32_e32 v142, s33, v208
	s_waitcnt vmcnt(9)
	ds_write_b128 v142, v[138:141] offset:8192
	s_waitcnt vmcnt(8)
	ds_write_b128 v142, v[146:149] offset:16384
	v_mfma_f32_32x32x16_f16 v[66:81], v[182:185], v[240:243], v[66:81]
	v_mfma_f32_32x32x16_f16 v[50:65], v[186:189], v[194:197], v[50:65]
	s_waitcnt vmcnt(7)
	ds_write_b128 v142, v[134:137] offset:24576
	s_waitcnt vmcnt(6)
	ds_write_b128 v142, v[130:133] offset:32768
	v_mfma_f32_32x32x16_f16 v[34:49], v[186:189], v[240:243], v[34:49]
	v_add_co_u32_e64 v130, s[0:1], s40, v202
	global_load_dwordx4 v[142:145], v[252:253], off offset:-16 sc1 nt
	global_load_dwordx4 v[150:153], v[204:205], off offset:-16 sc1 nt
	v_addc_co_u32_e64 v131, s[0:1], -1, v203, s[0:1]
	v_add_co_u32_e64 v132, s[0:1], s41, v202
	v_mfma_f32_32x32x16_f16 v[18:33], v[190:193], v[194:197], v[18:33]
	s_nop 0
	v_addc_co_u32_e64 v133, s[0:1], -1, v203, s[0:1]
	global_load_dwordx4 v[138:141], v[130:131], off sc1
	global_load_dwordx4 v[146:149], v[132:133], off sc1
	v_add_co_u32_e64 v130, s[0:1], s42, v202
	s_nop 1
	v_addc_co_u32_e64 v131, s[0:1], -1, v203, s[0:1]
	global_load_dwordx4 v[134:137], v[130:131], off sc1
	s_nop 0
	global_load_dwordx4 v[130:133], v[202:203], off sc1
	v_mfma_f32_32x32x16_f16 v[2:17], v[190:193], v[240:243], v[2:17]
	v_add_u32_e32 v178, s34, v216
	ds_read_b128 v[198:201], v178 offset:8192
	ds_read_b128 v[194:197], v178 offset:10240
	ds_read_b128 v[190:193], v178 offset:12288
	ds_read_b128 v[178:181], v178 offset:14336
	v_add_u32_e32 v182, s34, v217
	ds_read_b128 v[186:189], v182
	ds_read_b128 v[182:185], v182 offset:2048
	s_waitcnt lgkmcnt(12)
	v_mfma_f32_32x32x16_f16 v[114:129], v[220:223], v[236:239], v[114:129]
	s_waitcnt lgkmcnt(11)
	v_mfma_f32_32x32x16_f16 v[98:113], v[220:223], v[244:247], v[98:113]
	v_mfma_f32_32x32x16_f16 v[82:97], v[224:227], v[236:239], v[82:97]
	v_mfma_f32_32x32x16_f16 v[66:81], v[224:227], v[244:247], v[66:81]
	v_mfma_f32_32x32x16_f16 v[50:65], v[228:231], v[236:239], v[50:65]
	v_mfma_f32_32x32x16_f16 v[34:49], v[228:231], v[244:247], v[34:49]
	v_mfma_f32_32x32x16_f16 v[18:33], v[232:235], v[236:239], v[18:33]
	v_mfma_f32_32x32x16_f16 v[2:17], v[232:235], v[244:247], v[2:17]
	s_waitcnt lgkmcnt(0)
	s_barrier
	s_add_i32 s35, s35, 2
	v_lshl_add_u64 v[202:203], v[202:203], 0, s[24:25]
	v_lshl_add_u64 v[204:205], v[204:205], 0, s[26:27]
	v_lshl_add_u64 v[252:253], v[252:253], 0, s[26:27]
	s_mov_b32 s43, s34
	s_cmp_gt_u32 s35, 9
	s_mov_b32 s34, s44
	s_cbranch_scc0 .LBB1_1
	s_and_b64 s[0:1], s[20:21], exec
	s_cselect_b32 s6, s6, s8
	s_cselect_b32 s7, s7, s9
	s_and_b64 s[0:1], vcc, exec
	s_cselect_b32 s1, s5, s7
	s_cselect_b32 s0, s4, s6
	v_mov_b32_e32 v202, 0x3e38aa3b
	s_waitcnt lgkmcnt(1)
	v_mfma_f32_32x32x16_f16 v[114:129], v[198:201], v[186:189], v[114:129]
	v_cndmask_b32_e32 v202, 1.0, v202, vcc
	s_waitcnt lgkmcnt(0)
	v_mfma_f32_32x32x16_f16 v[98:113], v[198:201], v[182:185], v[98:113]
	ds_read_b128 v[198:201], v215 offset:8192
	ds_read_b128 v[220:223], v215 offset:10240
	ds_read_b128 v[224:227], v215 offset:12288
	ds_read_b128 v[228:231], v215 offset:14336
	ds_read_b128 v[232:235], v214
	ds_read_b128 v[236:239], v214 offset:2048
	s_waitcnt vmcnt(10)
	v_cvt_pk_f16_f32 v162, v162, v163
	v_cvt_pk_f16_f32 v163, v164, v165
	v_cvt_pk_f16_f32 v164, v154, v155
	v_cvt_pk_f16_f32 v165, v156, v157
	v_add_u32_e32 v154, 0x14000, v209
	ds_write_b64 v154, v[162:163]
	v_add_u32_e32 v154, 0x14000, v248
	ds_write_b64 v154, v[164:165]
	v_add_u32_e32 v154, 0x14000, v213
	s_waitcnt vmcnt(9)
	ds_write_b128 v154, v[158:161]
	v_add_u32_e32 v154, 0x16000, v213
	v_mfma_f32_32x32x16_f16 v[82:97], v[194:197], v[186:189], v[82:97]
	s_waitcnt vmcnt(8)
	ds_write_b128 v154, v[174:177]
	v_mfma_f32_32x32x16_f16 v[66:81], v[194:197], v[182:185], v[66:81]
	v_add_u32_e32 v154, 0x18000, v213
	s_waitcnt vmcnt(7)
	ds_write_b128 v154, v[166:169]
	v_add_u32_e32 v154, 0x1a000, v213
	v_mfma_f32_32x32x16_f16 v[50:65], v[190:193], v[186:189], v[50:65]
	s_waitcnt vmcnt(6)
	ds_write_b128 v154, v[170:173]
	v_mfma_f32_32x32x16_f16 v[34:49], v[190:193], v[182:185], v[34:49]
	v_mfma_f32_32x32x16_f16 v[18:33], v[178:181], v[186:189], v[18:33]
	v_mfma_f32_32x32x16_f16 v[2:17], v[178:181], v[182:185], v[2:17]
	ds_read_b128 v[154:157], v216 offset:49152
	ds_read_b128 v[158:161], v216 offset:51200
	ds_read_b128 v[162:165], v216 offset:53248
	ds_read_b128 v[166:169], v216 offset:55296
	ds_read_b128 v[170:173], v217 offset:40960
	ds_read_b128 v[174:177], v217 offset:43008
	s_waitcnt lgkmcnt(12)
	v_mfma_f32_32x32x16_f16 v[114:129], v[198:201], v[232:235], v[114:129]
	s_waitcnt lgkmcnt(11)
	v_mfma_f32_32x32x16_f16 v[98:113], v[198:201], v[236:239], v[98:113]
	v_mfma_f32_32x32x16_f16 v[82:97], v[220:223], v[232:235], v[82:97]
	v_mfma_f32_32x32x16_f16 v[66:81], v[220:223], v[236:239], v[66:81]
	v_mfma_f32_32x32x16_f16 v[50:65], v[224:227], v[232:235], v[50:65]
	v_mfma_f32_32x32x16_f16 v[34:49], v[224:227], v[236:239], v[34:49]
	v_mfma_f32_32x32x16_f16 v[18:33], v[228:231], v[232:235], v[18:33]
	v_mfma_f32_32x32x16_f16 v[2:17], v[228:231], v[236:239], v[2:17]
	s_waitcnt lgkmcnt(0)
	s_barrier
	s_waitcnt lgkmcnt(1)
	v_mfma_f32_32x32x16_f16 v[114:129], v[154:157], v[170:173], v[114:129]
	s_waitcnt lgkmcnt(0)
	v_mfma_f32_32x32x16_f16 v[98:113], v[154:157], v[174:177], v[98:113]
	ds_read_b128 v[154:157], v215 offset:49152
	ds_read_b128 v[178:181], v215 offset:51200
	ds_read_b128 v[182:185], v215 offset:53248
	ds_read_b128 v[186:189], v215 offset:55296
	ds_read_b128 v[190:193], v214 offset:40960
	ds_read_b128 v[194:197], v214 offset:43008
	s_waitcnt vmcnt(4)
	v_cvt_pk_f16_f32 v150, v150, v151
	v_cvt_pk_f16_f32 v151, v152, v153
	v_cvt_pk_f16_f32 v152, v142, v143
	v_cvt_pk_f16_f32 v153, v144, v145
	ds_write_b64 v209, v[150:151]
	ds_write_b64 v248, v[152:153]
	v_mfma_f32_32x32x16_f16 v[82:97], v[158:161], v[170:173], v[82:97]
	s_waitcnt vmcnt(3)
	ds_write_b128 v208, v[138:141] offset:8192
	s_waitcnt vmcnt(2)
	ds_write_b128 v208, v[146:149] offset:16384
	v_mfma_f32_32x32x16_f16 v[66:81], v[158:161], v[174:177], v[66:81]
	v_mfma_f32_32x32x16_f16 v[50:65], v[162:165], v[170:173], v[50:65]
	s_waitcnt vmcnt(1)
	ds_write_b128 v208, v[134:137] offset:24576
	s_waitcnt vmcnt(0)
	ds_write_b128 v208, v[130:133] offset:32768
	v_mfma_f32_32x32x16_f16 v[34:49], v[162:165], v[174:177], v[34:49]
	v_mfma_f32_32x32x16_f16 v[18:33], v[166:169], v[170:173], v[18:33]
	v_mfma_f32_32x32x16_f16 v[2:17], v[166:169], v[174:177], v[2:17]
	v_add_u32_e32 v158, 0x16000, v211
	v_add_u32_e32 v142, v158, v210
	ds_read_b128 v[130:133], v142
	ds_read_b128 v[134:137], v142 offset:2048
	ds_read_b128 v[138:141], v142 offset:4096
	ds_read_b128 v[142:145], v142 offset:6144
	v_add_u32_e32 v166, 0x14000, v218
	v_add_u32_e32 v150, v166, v210
	ds_read_b128 v[146:149], v150
	ds_read_b128 v[150:153], v150 offset:2048
	s_waitcnt lgkmcnt(12)
	v_mfma_f32_32x32x16_f16 v[114:129], v[154:157], v[190:193], v[114:129]
	s_waitcnt lgkmcnt(11)
	v_mfma_f32_32x32x16_f16 v[98:113], v[154:157], v[194:197], v[98:113]
	v_mfma_f32_32x32x16_f16 v[82:97], v[178:181], v[190:193], v[82:97]
	v_mfma_f32_32x32x16_f16 v[66:81], v[178:181], v[194:197], v[66:81]
	v_mfma_f32_32x32x16_f16 v[50:65], v[182:185], v[190:193], v[50:65]
	v_mfma_f32_32x32x16_f16 v[34:49], v[182:185], v[194:197], v[34:49]
	v_mfma_f32_32x32x16_f16 v[18:33], v[186:189], v[190:193], v[18:33]
	v_mfma_f32_32x32x16_f16 v[2:17], v[186:189], v[194:197], v[2:17]
	s_waitcnt lgkmcnt(0)
	s_barrier
	s_waitcnt lgkmcnt(1)
	v_mfma_f32_32x32x16_f16 v[114:129], v[130:133], v[146:149], v[114:129]
	s_waitcnt lgkmcnt(0)
	v_mfma_f32_32x32x16_f16 v[98:113], v[130:133], v[150:153], v[98:113]
	v_add_u32_e32 v162, v158, v212
	ds_read_b128 v[130:133], v162
	ds_read_b128 v[154:157], v162 offset:2048
	ds_read_b128 v[158:161], v162 offset:4096
	ds_read_b128 v[162:165], v162 offset:6144
	v_add_u32_e32 v170, v166, v212
	ds_read_b128 v[166:169], v170
	ds_read_b128 v[170:173], v170 offset:2048
	v_mfma_f32_32x32x16_f16 v[82:97], v[134:137], v[146:149], v[82:97]
	v_mfma_f32_32x32x16_f16 v[66:81], v[134:137], v[150:153], v[66:81]
	v_mfma_f32_32x32x16_f16 v[50:65], v[138:141], v[146:149], v[50:65]
	v_mfma_f32_32x32x16_f16 v[34:49], v[138:141], v[150:153], v[34:49]
	v_mfma_f32_32x32x16_f16 v[18:33], v[142:145], v[146:149], v[18:33]
	v_mfma_f32_32x32x16_f16 v[2:17], v[142:145], v[150:153], v[2:17]
	ds_read_b128 v[134:137], v216 offset:8192
	ds_read_b128 v[138:141], v216 offset:10240
	ds_read_b128 v[142:145], v216 offset:12288
	ds_read_b128 v[146:149], v216 offset:14336
	ds_read_b128 v[150:153], v217
	ds_read_b128 v[174:177], v217 offset:2048
	s_waitcnt lgkmcnt(7)
	v_mfma_f32_32x32x16_f16 v[114:129], v[130:133], v[166:169], v[114:129]
	s_waitcnt lgkmcnt(6)
	v_mfma_f32_32x32x16_f16 v[98:113], v[130:133], v[170:173], v[98:113]
	v_mfma_f32_32x32x16_f16 v[82:97], v[154:157], v[166:169], v[82:97]
	v_mfma_f32_32x32x16_f16 v[66:81], v[154:157], v[170:173], v[66:81]
	v_mfma_f32_32x32x16_f16 v[50:65], v[158:161], v[166:169], v[50:65]
	v_mfma_f32_32x32x16_f16 v[34:49], v[158:161], v[170:173], v[34:49]
	v_mfma_f32_32x32x16_f16 v[18:33], v[162:165], v[166:169], v[18:33]
	v_mfma_f32_32x32x16_f16 v[2:17], v[162:165], v[170:173], v[2:17]
	s_waitcnt lgkmcnt(0)
	s_barrier
	s_waitcnt lgkmcnt(1)
	v_mfma_f32_32x32x16_f16 v[114:129], v[134:137], v[150:153], v[114:129]
	s_waitcnt lgkmcnt(0)
	v_mfma_f32_32x32x16_f16 v[98:113], v[134:137], v[174:177], v[98:113]
	ds_read_b128 v[130:133], v215 offset:8192
	ds_read_b128 v[134:137], v215 offset:10240
	ds_read_b128 v[154:157], v215 offset:12288
	ds_read_b128 v[158:161], v215 offset:14336
	ds_read_b128 v[162:165], v214
	ds_read_b128 v[166:169], v214 offset:2048
	v_mfma_f32_32x32x16_f16 v[82:97], v[138:141], v[150:153], v[82:97]
	v_mfma_f32_32x32x16_f16 v[66:81], v[138:141], v[174:177], v[66:81]
	v_mfma_f32_32x32x16_f16 v[50:65], v[142:145], v[150:153], v[50:65]
	v_mfma_f32_32x32x16_f16 v[34:49], v[142:145], v[174:177], v[34:49]
	v_mfma_f32_32x32x16_f16 v[18:33], v[146:149], v[150:153], v[18:33]
	v_mfma_f32_32x32x16_f16 v[2:17], v[146:149], v[174:177], v[2:17]
	s_waitcnt lgkmcnt(1)
	v_mfma_f32_32x32x16_f16 v[114:129], v[130:133], v[162:165], v[114:129]
	s_waitcnt lgkmcnt(0)
	v_mfma_f32_32x32x16_f16 v[98:113], v[130:133], v[166:169], v[98:113]
	v_mfma_f32_32x32x16_f16 v[82:97], v[134:137], v[162:165], v[82:97]
	v_mfma_f32_32x32x16_f16 v[66:81], v[134:137], v[166:169], v[66:81]
	v_mfma_f32_32x32x16_f16 v[50:65], v[154:157], v[162:165], v[50:65]
	v_mfma_f32_32x32x16_f16 v[34:49], v[154:157], v[166:169], v[34:49]
	v_mfma_f32_32x32x16_f16 v[18:33], v[158:161], v[162:165], v[18:33]
	v_mfma_f32_32x32x16_f16 v[2:17], v[158:161], v[166:169], v[2:17]
	v_lshl_or_b32 v130, v207, 2, s31
	s_waitcnt lgkmcnt(0)
	s_barrier
	s_cbranch_vccnz .Lepi_q
	v_lshlrev_b32_e32 v154, 2, v130
	global_load_dwordx4 v[134:137], v154, s[0:1]
	global_load_dwordx4 v[150:153], v154, s[0:1] offset:32
	global_load_dwordx4 v[156:159], v154, s[0:1] offset:64
	global_load_dwordx4 v[160:163], v154, s[0:1] offset:96
	global_load_dwordx4 v[164:167], v154, s[0:1] offset:128
	global_load_dwordx4 v[168:171], v154, s[0:1] offset:160
	s_movk_i32 s4, 0x410
	v_lshlrev_b32_e32 v130, 1, v130
	v_mul_lo_u32 v131, v206, s4
	v_add3_u32 v155, 0, v130, v131
	global_load_dwordx4 v[172:175], v154, s[0:1] offset:192
	global_load_dwordx4 v[146:149], v154, s[0:1] offset:224
	global_load_dwordx4 v[142:145], v154, s[0:1] offset:256
	global_load_dwordx4 v[130:133], v154, s[0:1] offset:288
	global_load_dwordx4 v[138:141], v154, s[0:1] offset:320
	v_add_u32_e32 v176, 0x8000, v155
	s_waitcnt vmcnt(10)
	v_pk_add_f32 v[114:115], v[134:135], v[114:115]
	v_pk_add_f32 v[116:117], v[136:137], v[116:117]
	v_pk_add_f32 v[98:99], v[134:135], v[98:99]
	v_pk_add_f32 v[100:101], v[136:137], v[100:101]
	s_waitcnt vmcnt(9)
	v_pk_add_f32 v[118:119], v[150:151], v[118:119]
	v_pk_add_f32 v[120:121], v[152:153], v[120:121]
	s_waitcnt vmcnt(6)
	v_pk_add_f32 v[82:83], v[164:165], v[82:83]
	v_pk_add_f32 v[84:85], v[166:167], v[84:85]
	v_pk_add_f32 v[66:67], v[164:165], v[66:67]
	v_pk_add_f32 v[68:69], v[166:167], v[68:69]
	s_waitcnt vmcnt(5)
	v_pk_add_f32 v[70:71], v[168:169], v[70:71]
	v_pk_add_f32 v[72:73], v[170:171], v[72:73]
	v_pk_add_f32 v[102:103], v[150:151], v[102:103]
	v_pk_add_f32 v[104:105], v[152:153], v[104:105]
	v_pk_add_f32 v[122:123], v[156:157], v[122:123]
	v_pk_add_f32 v[124:125], v[158:159], v[124:125]
	v_pk_add_f32 v[106:107], v[156:157], v[106:107]
	v_pk_add_f32 v[108:109], v[158:159], v[108:109]
	v_pk_add_f32 v[126:127], v[160:161], v[126:127]
	v_pk_add_f32 v[128:129], v[162:163], v[128:129]
	v_pk_add_f32 v[110:111], v[160:161], v[110:111]
	v_pk_add_f32 v[112:113], v[162:163], v[112:113]
	v_pk_add_f32 v[86:87], v[168:169], v[86:87]
	v_pk_add_f32 v[88:89], v[170:171], v[88:89]
	v_cvt_pk_f16_f32 v114, v114, v115
	v_cvt_pk_f16_f32 v115, v116, v117
	v_cvt_pk_f16_f32 v98, v98, v99
	v_cvt_pk_f16_f32 v99, v100, v101
	v_cvt_pk_f16_f32 v100, v118, v119
	v_cvt_pk_f16_f32 v101, v120, v121
	v_cvt_pk_f16_f32 v82, v82, v83
	v_cvt_pk_f16_f32 v83, v84, v85
	v_cvt_pk_f16_f32 v84, v66, v67
	v_cvt_pk_f16_f32 v85, v68, v69
	v_cvt_pk_f16_f32 v70, v70, v71
	v_cvt_pk_f16_f32 v71, v72, v73
	v_cvt_pk_f16_f32 v102, v102, v103
	v_cvt_pk_f16_f32 v103, v104, v105
	v_cvt_pk_f16_f32 v104, v122, v123
	v_cvt_pk_f16_f32 v105, v124, v125
	v_cvt_pk_f16_f32 v106, v106, v107
	v_cvt_pk_f16_f32 v107, v108, v109
	v_cvt_pk_f16_f32 v108, v126, v127
	v_cvt_pk_f16_f32 v109, v128, v129
	v_cvt_pk_f16_f32 v110, v110, v111
	v_cvt_pk_f16_f32 v111, v112, v113
	v_cvt_pk_f16_f32 v86, v86, v87
	ds_write2_b64 v155, v[114:115], v[100:101] offset1:2
	ds_write2_b64 v176, v[98:99], v[102:103] offset0:64 offset1:66
	ds_write2_b64 v155, v[104:105], v[108:109] offset0:4 offset1:6
	ds_write2_b64 v176, v[106:107], v[110:111] offset0:68 offset1:70
	v_cvt_pk_f16_f32 v87, v88, v89
	ds_write2_b64 v176, v[84:85], v[70:71] offset0:72 offset1:74
	s_waitcnt vmcnt(4)
	v_pk_add_f32 v[70:71], v[172:173], v[90:91]
	v_pk_add_f32 v[84:85], v[174:175], v[92:93]
	v_pk_add_f32 v[74:75], v[172:173], v[74:75]
	ds_write2_b64 v155, v[82:83], v[86:87] offset0:8 offset1:10
	v_mov_b64_e32 v[82:83], v[70:71]
	global_load_dwordx4 v[66:69], v154, s[0:1] offset:352
	global_load_dwordx4 v[70:73], v154, s[0:1] offset:384
	v_cvt_pk_f16_f32 v82, v82, v83
	v_cvt_pk_f16_f32 v83, v84, v85
	v_cvt_pk_f16_f32 v84, v74, v75
	v_pk_add_f32 v[74:75], v[174:175], v[76:77]
	s_waitcnt vmcnt(5)
	v_pk_add_f32 v[78:79], v[146:147], v[78:79]
	v_cvt_pk_f16_f32 v85, v74, v75
	global_load_dwordx4 v[74:77], v154, s[0:1] offset:416
	v_pk_add_f32 v[80:81], v[148:149], v[80:81]
	v_cvt_pk_f16_f32 v78, v78, v79
	v_cvt_pk_f16_f32 v79, v80, v81
	ds_write2_b64 v176, v[84:85], v[78:79] offset0:76 offset1:78
	global_load_dwordx4 v[78:81], v154, s[0:1] offset:448
	v_pk_add_f32 v[86:87], v[146:147], v[94:95]
	v_pk_add_f32 v[88:89], v[148:149], v[96:97]
	s_waitcnt vmcnt(6)
	v_pk_add_f32 v[50:51], v[142:143], v[50:51]
	v_pk_add_f32 v[52:53], v[144:145], v[52:53]
	v_pk_add_f32 v[34:35], v[142:143], v[34:35]
	v_cvt_pk_f16_f32 v86, v86, v87
	v_cvt_pk_f16_f32 v87, v88, v89
	v_cvt_pk_f16_f32 v50, v50, v51
	v_cvt_pk_f16_f32 v51, v52, v53
	v_cvt_pk_f16_f32 v52, v34, v35
	v_pk_add_f32 v[34:35], v[144:145], v[36:37]
	ds_write2_b64 v155, v[82:83], v[86:87] offset0:12 offset1:14
	v_mov_b64_e32 v[82:83], v[34:35]
	global_load_dwordx4 v[34:37], v154, s[0:1] offset:480
	s_waitcnt vmcnt(6)
	v_pk_add_f32 v[38:39], v[130:131], v[38:39]
	v_pk_add_f32 v[40:41], v[132:133], v[40:41]
	v_cvt_pk_f16_f32 v53, v82, v83
	v_cvt_pk_f16_f32 v38, v38, v39
	v_cvt_pk_f16_f32 v39, v40, v41
	ds_write2_b64 v176, v[52:53], v[38:39] offset0:80 offset1:82
	s_waitcnt vmcnt(5)
	v_pk_add_f32 v[38:39], v[138:139], v[58:59]
	v_pk_add_f32 v[40:41], v[140:141], v[60:61]
	v_cvt_pk_f16_f32 v38, v38, v39
	v_cvt_pk_f16_f32 v39, v40, v41
	v_pk_add_f32 v[40:41], v[138:139], v[42:43]
	v_pk_add_f32 v[42:43], v[140:141], v[44:45]
	v_cvt_pk_f16_f32 v40, v40, v41
	v_cvt_pk_f16_f32 v41, v42, v43
	v_pk_add_f32 v[54:55], v[130:131], v[54:55]
	v_pk_add_f32 v[56:57], v[132:133], v[56:57]
	v_cmp_gt_u32_e64 s[0:1], 8, v0
	v_cvt_pk_f16_f32 v54, v54, v55
	v_cvt_pk_f16_f32 v55, v56, v57
	s_and_b64 s[6:7], s[20:21], s[0:1]
	ds_write2_b64 v155, v[50:51], v[54:55] offset0:16 offset1:18
	s_waitcnt vmcnt(4)
	v_pk_add_f32 v[42:43], v[66:67], v[62:63]
	s_waitcnt vmcnt(3)
	v_pk_add_f32 v[18:19], v[70:71], v[18:19]
	v_pk_add_f32 v[20:21], v[72:73], v[20:21]
	v_pk_add_f32 v[2:3], v[70:71], v[2:3]
	v_pk_add_f32 v[4:5], v[72:73], v[4:5]
	v_cvt_pk_f16_f32 v18, v18, v19
	v_cvt_pk_f16_f32 v19, v20, v21
	v_cvt_pk_f16_f32 v2, v2, v3
	v_cvt_pk_f16_f32 v3, v4, v5
	s_waitcnt vmcnt(2)
	v_pk_add_f32 v[4:5], v[74:75], v[22:23]
	v_pk_add_f32 v[20:21], v[76:77], v[24:25]
	v_cvt_pk_f16_f32 v4, v4, v5
	v_cvt_pk_f16_f32 v5, v20, v21
	ds_write2_b64 v155, v[18:19], v[4:5] offset0:24 offset1:26
	v_pk_add_f32 v[4:5], v[74:75], v[6:7]
	v_pk_add_f32 v[6:7], v[76:77], v[8:9]
	v_cvt_pk_f16_f32 v4, v4, v5
	v_cvt_pk_f16_f32 v5, v6, v7
	ds_write2_b64 v176, v[2:3], v[4:5] offset0:88 offset1:90
	s_waitcnt vmcnt(1)
	v_pk_add_f32 v[2:3], v[78:79], v[26:27]
	v_pk_add_f32 v[4:5], v[80:81], v[28:29]
	v_cvt_pk_f16_f32 v2, v2, v3
	v_cvt_pk_f16_f32 v3, v4, v5
	v_pk_add_f32 v[4:5], v[78:79], v[10:11]
	v_pk_add_f32 v[6:7], v[80:81], v[12:13]
	v_pk_add_f32 v[44:45], v[68:69], v[64:65]
	v_cvt_pk_f16_f32 v4, v4, v5
	v_cvt_pk_f16_f32 v5, v6, v7
	s_waitcnt vmcnt(0)
	v_pk_add_f32 v[6:7], v[34:35], v[30:31]
	v_pk_add_f32 v[8:9], v[36:37], v[32:33]
	v_cvt_pk_f16_f32 v42, v42, v43
	v_cvt_pk_f16_f32 v43, v44, v45
	v_cvt_pk_f16_f32 v6, v6, v7
	v_cvt_pk_f16_f32 v7, v8, v9
	ds_write2_b64 v155, v[38:39], v[42:43] offset0:20 offset1:22
	v_pk_add_f32 v[38:39], v[66:67], v[46:47]
	v_pk_add_f32 v[42:43], v[68:69], v[48:49]
	ds_write2_b64 v155, v[2:3], v[6:7] offset0:28 offset1:30
	v_pk_add_f32 v[2:3], v[34:35], v[14:15]
	v_pk_add_f32 v[6:7], v[36:37], v[16:17]
	v_cvt_pk_f16_f32 v38, v38, v39
	v_cvt_pk_f16_f32 v39, v42, v43
	v_cvt_pk_f16_f32 v2, v2, v3
	v_cvt_pk_f16_f32 v3, v6, v7
	ds_write2_b64 v176, v[40:41], v[38:39] offset0:84 offset1:86
	ds_write2_b64 v176, v[4:5], v[2:3] offset0:92 offset1:94
	s_branch .Lepi_join
.Lepi_q:
	v_lshlrev_b32_e32 v154, 2, v130
	global_load_dwordx4 v[134:137], v154, s[0:1]
	global_load_dwordx4 v[150:153], v154, s[0:1] offset:32
	global_load_dwordx4 v[156:159], v154, s[0:1] offset:64
	global_load_dwordx4 v[160:163], v154, s[0:1] offset:96
	global_load_dwordx4 v[164:167], v154, s[0:1] offset:128
	global_load_dwordx4 v[168:171], v154, s[0:1] offset:160
	s_movk_i32 s4, 0x410
	v_lshlrev_b32_e32 v130, 1, v130
	v_mul_lo_u32 v131, v206, s4
	v_add3_u32 v155, 0, v130, v131
	global_load_dwordx4 v[172:175], v154, s[0:1] offset:192
	global_load_dwordx4 v[146:149], v154, s[0:1] offset:224
	global_load_dwordx4 v[142:145], v154, s[0:1] offset:256
	global_load_dwordx4 v[130:133], v154, s[0:1] offset:288
	global_load_dwordx4 v[138:141], v154, s[0:1] offset:320
	v_add_u32_e32 v176, 0x8000, v155
	s_waitcnt vmcnt(10)
	v_pk_add_f32 v[114:115], v[134:135], v[114:115]
	v_pk_add_f32 v[116:117], v[136:137], v[116:117]
	v_pk_add_f32 v[98:99], v[134:135], v[98:99]
	v_pk_add_f32 v[100:101], v[136:137], v[100:101]
	s_waitcnt vmcnt(9)
	v_pk_add_f32 v[118:119], v[150:151], v[118:119]
	v_pk_add_f32 v[120:121], v[152:153], v[120:121]
	s_waitcnt vmcnt(6)
	v_pk_add_f32 v[82:83], v[164:165], v[82:83]
	v_pk_add_f32 v[84:85], v[166:167], v[84:85]
	v_pk_add_f32 v[66:67], v[164:165], v[66:67]
	v_pk_add_f32 v[68:69], v[166:167], v[68:69]
	s_waitcnt vmcnt(5)
	v_pk_add_f32 v[70:71], v[168:169], v[70:71]
	v_pk_add_f32 v[72:73], v[170:171], v[72:73]
	v_pk_add_f32 v[102:103], v[150:151], v[102:103]
	v_pk_add_f32 v[104:105], v[152:153], v[104:105]
	v_pk_add_f32 v[122:123], v[156:157], v[122:123]
	v_pk_add_f32 v[124:125], v[158:159], v[124:125]
	v_pk_add_f32 v[106:107], v[156:157], v[106:107]
	v_pk_add_f32 v[108:109], v[158:159], v[108:109]
	v_pk_add_f32 v[126:127], v[160:161], v[126:127]
	v_pk_add_f32 v[128:129], v[162:163], v[128:129]
	v_pk_add_f32 v[110:111], v[160:161], v[110:111]
	v_pk_add_f32 v[112:113], v[162:163], v[112:113]
	v_pk_add_f32 v[86:87], v[168:169], v[86:87]
	v_pk_mul_f32 v[114:115], v[202:203], v[114:115] op_sel_hi:[0,1]
	v_pk_mul_f32 v[116:117], v[202:203], v[116:117] op_sel_hi:[0,1]
	v_pk_mul_f32 v[98:99], v[202:203], v[98:99] op_sel_hi:[0,1]
	v_pk_mul_f32 v[100:101], v[202:203], v[100:101] op_sel_hi:[0,1]
	v_pk_mul_f32 v[118:119], v[202:203], v[118:119] op_sel_hi:[0,1]
	v_pk_mul_f32 v[120:121], v[202:203], v[120:121] op_sel_hi:[0,1]
	v_pk_mul_f32 v[82:83], v[202:203], v[82:83] op_sel_hi:[0,1]
	v_pk_mul_f32 v[84:85], v[202:203], v[84:85] op_sel_hi:[0,1]
	v_pk_mul_f32 v[66:67], v[202:203], v[66:67] op_sel_hi:[0,1]
	v_pk_mul_f32 v[68:69], v[202:203], v[68:69] op_sel_hi:[0,1]
	v_pk_add_f32 v[88:89], v[170:171], v[88:89]
	v_pk_mul_f32 v[70:71], v[202:203], v[70:71] op_sel_hi:[0,1]
	v_pk_mul_f32 v[72:73], v[202:203], v[72:73] op_sel_hi:[0,1]
	v_pk_mul_f32 v[102:103], v[202:203], v[102:103] op_sel_hi:[0,1]
	v_pk_mul_f32 v[104:105], v[202:203], v[104:105] op_sel_hi:[0,1]
	v_pk_mul_f32 v[122:123], v[202:203], v[122:123] op_sel_hi:[0,1]
	v_pk_mul_f32 v[124:125], v[202:203], v[124:125] op_sel_hi:[0,1]
	v_pk_mul_f32 v[106:107], v[202:203], v[106:107] op_sel_hi:[0,1]
	v_pk_mul_f32 v[108:109], v[202:203], v[108:109] op_sel_hi:[0,1]
	v_pk_mul_f32 v[126:127], v[202:203], v[126:127] op_sel_hi:[0,1]
	v_pk_mul_f32 v[128:129], v[202:203], v[128:129] op_sel_hi:[0,1]
	v_pk_mul_f32 v[110:111], v[202:203], v[110:111] op_sel_hi:[0,1]
	v_pk_mul_f32 v[112:113], v[202:203], v[112:113] op_sel_hi:[0,1]
	v_pk_mul_f32 v[86:87], v[202:203], v[86:87] op_sel_hi:[0,1]
	v_cvt_pk_f16_f32 v114, v114, v115
	v_cvt_pk_f16_f32 v115, v116, v117
	v_cvt_pk_f16_f32 v98, v98, v99
	v_cvt_pk_f16_f32 v99, v100, v101
	v_cvt_pk_f16_f32 v100, v118, v119
	v_cvt_pk_f16_f32 v101, v120, v121
	v_cvt_pk_f16_f32 v82, v82, v83
	v_cvt_pk_f16_f32 v83, v84, v85
	v_cvt_pk_f16_f32 v84, v66, v67
	v_cvt_pk_f16_f32 v85, v68, v69
	v_pk_mul_f32 v[88:89], v[202:203], v[88:89] op_sel_hi:[0,1]
	v_cvt_pk_f16_f32 v70, v70, v71
	v_cvt_pk_f16_f32 v71, v72, v73
	v_cvt_pk_f16_f32 v102, v102, v103
	v_cvt_pk_f16_f32 v103, v104, v105
	v_cvt_pk_f16_f32 v104, v122, v123
	v_cvt_pk_f16_f32 v105, v124, v125
	v_cvt_pk_f16_f32 v106, v106, v107
	v_cvt_pk_f16_f32 v107, v108, v109
	v_cvt_pk_f16_f32 v108, v126, v127
	v_cvt_pk_f16_f32 v109, v128, v129
	v_cvt_pk_f16_f32 v110, v110, v111
	v_cvt_pk_f16_f32 v111, v112, v113
	v_cvt_pk_f16_f32 v86, v86, v87
	ds_write2_b64 v155, v[114:115], v[100:101] offset1:2
	ds_write2_b64 v176, v[98:99], v[102:103] offset0:64 offset1:66
	ds_write2_b64 v155, v[104:105], v[108:109] offset0:4 offset1:6
	ds_write2_b64 v176, v[106:107], v[110:111] offset0:68 offset1:70
	v_cvt_pk_f16_f32 v87, v88, v89
	ds_write2_b64 v176, v[84:85], v[70:71] offset0:72 offset1:74
	s_waitcnt vmcnt(4)
	v_pk_add_f32 v[70:71], v[172:173], v[90:91]
	v_pk_add_f32 v[84:85], v[174:175], v[92:93]
	v_pk_add_f32 v[74:75], v[172:173], v[74:75]
	ds_write2_b64 v155, v[82:83], v[86:87] offset0:8 offset1:10
	v_pk_mul_f32 v[82:83], v[202:203], v[70:71] op_sel_hi:[0,1]
	v_pk_mul_f32 v[84:85], v[202:203], v[84:85] op_sel_hi:[0,1]
	v_pk_mul_f32 v[74:75], v[202:203], v[74:75] op_sel_hi:[0,1]
	global_load_dwordx4 v[66:69], v154, s[0:1] offset:352
	global_load_dwordx4 v[70:73], v154, s[0:1] offset:384
	v_cvt_pk_f16_f32 v82, v82, v83
	v_cvt_pk_f16_f32 v83, v84, v85
	v_cvt_pk_f16_f32 v84, v74, v75
	v_pk_add_f32 v[74:75], v[174:175], v[76:77]
	s_waitcnt vmcnt(5)
	v_pk_add_f32 v[78:79], v[146:147], v[78:79]
	v_pk_mul_f32 v[74:75], v[202:203], v[74:75] op_sel_hi:[0,1]
	v_cvt_pk_f16_f32 v85, v74, v75
	global_load_dwordx4 v[74:77], v154, s[0:1] offset:416
	v_pk_add_f32 v[80:81], v[148:149], v[80:81]
	v_pk_mul_f32 v[78:79], v[202:203], v[78:79] op_sel_hi:[0,1]
	v_pk_mul_f32 v[80:81], v[202:203], v[80:81] op_sel_hi:[0,1]
	v_cvt_pk_f16_f32 v78, v78, v79
	v_cvt_pk_f16_f32 v79, v80, v81
	ds_write2_b64 v176, v[84:85], v[78:79] offset0:76 offset1:78
	global_load_dwordx4 v[78:81], v154, s[0:1] offset:448
	v_pk_add_f32 v[86:87], v[146:147], v[94:95]
	v_pk_add_f32 v[88:89], v[148:149], v[96:97]
	s_waitcnt vmcnt(6)
	v_pk_add_f32 v[50:51], v[142:143], v[50:51]
	v_pk_add_f32 v[52:53], v[144:145], v[52:53]
	v_pk_add_f32 v[34:35], v[142:143], v[34:35]
	v_pk_mul_f32 v[86:87], v[202:203], v[86:87] op_sel_hi:[0,1]
	v_pk_mul_f32 v[88:89], v[202:203], v[88:89] op_sel_hi:[0,1]
	v_pk_mul_f32 v[50:51], v[202:203], v[50:51] op_sel_hi:[0,1]
	v_pk_mul_f32 v[52:53], v[202:203], v[52:53] op_sel_hi:[0,1]
	v_pk_mul_f32 v[34:35], v[202:203], v[34:35] op_sel_hi:[0,1]
	v_cvt_pk_f16_f32 v86, v86, v87
	v_cvt_pk_f16_f32 v87, v88, v89
	v_cvt_pk_f16_f32 v50, v50, v51
	v_cvt_pk_f16_f32 v51, v52, v53
	v_cvt_pk_f16_f32 v52, v34, v35
	v_pk_add_f32 v[34:35], v[144:145], v[36:37]
	ds_write2_b64 v155, v[82:83], v[86:87] offset0:12 offset1:14
	v_pk_mul_f32 v[82:83], v[202:203], v[34:35] op_sel_hi:[0,1]
	global_load_dwordx4 v[34:37], v154, s[0:1] offset:480
	s_waitcnt vmcnt(6)
	v_pk_add_f32 v[38:39], v[130:131], v[38:39]
	v_pk_add_f32 v[40:41], v[132:133], v[40:41]
	v_pk_mul_f32 v[38:39], v[202:203], v[38:39] op_sel_hi:[0,1]
	v_pk_mul_f32 v[40:41], v[202:203], v[40:41] op_sel_hi:[0,1]
	v_cvt_pk_f16_f32 v53, v82, v83
	v_cvt_pk_f16_f32 v38, v38, v39
	v_cvt_pk_f16_f32 v39, v40, v41
	ds_write2_b64 v176, v[52:53], v[38:39] offset0:80 offset1:82
	s_waitcnt vmcnt(5)
	v_pk_add_f32 v[38:39], v[138:139], v[58:59]
	v_pk_add_f32 v[40:41], v[140:141], v[60:61]
	v_pk_mul_f32 v[38:39], v[202:203], v[38:39] op_sel_hi:[0,1]
	v_pk_mul_f32 v[40:41], v[202:203], v[40:41] op_sel_hi:[0,1]
	v_cvt_pk_f16_f32 v38, v38, v39
	v_cvt_pk_f16_f32 v39, v40, v41
	v_pk_add_f32 v[40:41], v[138:139], v[42:43]
	v_pk_add_f32 v[42:43], v[140:141], v[44:45]
	v_pk_mul_f32 v[40:41], v[202:203], v[40:41] op_sel_hi:[0,1]
	v_pk_mul_f32 v[42:43], v[202:203], v[42:43] op_sel_hi:[0,1]
	v_cvt_pk_f16_f32 v40, v40, v41
	v_cvt_pk_f16_f32 v41, v42, v43
	v_pk_add_f32 v[54:55], v[130:131], v[54:55]
	v_pk_add_f32 v[56:57], v[132:133], v[56:57]
	v_pk_mul_f32 v[54:55], v[202:203], v[54:55] op_sel_hi:[0,1]
	v_pk_mul_f32 v[56:57], v[202:203], v[56:57] op_sel_hi:[0,1]
	v_cmp_gt_u32_e64 s[0:1], 8, v0
	v_cvt_pk_f16_f32 v54, v54, v55
	v_cvt_pk_f16_f32 v55, v56, v57
	s_and_b64 s[6:7], s[20:21], s[0:1]
	ds_write2_b64 v155, v[50:51], v[54:55] offset0:16 offset1:18
	s_waitcnt vmcnt(4)
	v_pk_add_f32 v[42:43], v[66:67], v[62:63]
	s_waitcnt vmcnt(3)
	v_pk_add_f32 v[18:19], v[70:71], v[18:19]
	v_pk_add_f32 v[20:21], v[72:73], v[20:21]
	v_pk_add_f32 v[2:3], v[70:71], v[2:3]
	v_pk_add_f32 v[4:5], v[72:73], v[4:5]
	v_pk_mul_f32 v[18:19], v[202:203], v[18:19] op_sel_hi:[0,1]
	v_pk_mul_f32 v[20:21], v[202:203], v[20:21] op_sel_hi:[0,1]
	v_pk_mul_f32 v[2:3], v[202:203], v[2:3] op_sel_hi:[0,1]
	v_pk_mul_f32 v[4:5], v[202:203], v[4:5] op_sel_hi:[0,1]
	v_cvt_pk_f16_f32 v18, v18, v19
	v_cvt_pk_f16_f32 v19, v20, v21
	v_cvt_pk_f16_f32 v2, v2, v3
	v_cvt_pk_f16_f32 v3, v4, v5
	s_waitcnt vmcnt(2)
	v_pk_add_f32 v[4:5], v[74:75], v[22:23]
	v_pk_add_f32 v[20:21], v[76:77], v[24:25]
	v_pk_mul_f32 v[4:5], v[202:203], v[4:5] op_sel_hi:[0,1]
	v_pk_mul_f32 v[20:21], v[202:203], v[20:21] op_sel_hi:[0,1]
	v_cvt_pk_f16_f32 v4, v4, v5
	v_cvt_pk_f16_f32 v5, v20, v21
	ds_write2_b64 v155, v[18:19], v[4:5] offset0:24 offset1:26
	v_pk_add_f32 v[4:5], v[74:75], v[6:7]
	v_pk_add_f32 v[6:7], v[76:77], v[8:9]
	v_pk_mul_f32 v[4:5], v[202:203], v[4:5] op_sel_hi:[0,1]
	v_pk_mul_f32 v[6:7], v[202:203], v[6:7] op_sel_hi:[0,1]
	v_cvt_pk_f16_f32 v4, v4, v5
	v_cvt_pk_f16_f32 v5, v6, v7
	ds_write2_b64 v176, v[2:3], v[4:5] offset0:88 offset1:90
	s_waitcnt vmcnt(1)
	v_pk_add_f32 v[2:3], v[78:79], v[26:27]
	v_pk_add_f32 v[4:5], v[80:81], v[28:29]
	v_pk_mul_f32 v[2:3], v[202:203], v[2:3] op_sel_hi:[0,1]
	v_pk_mul_f32 v[4:5], v[202:203], v[4:5] op_sel_hi:[0,1]
	v_cvt_pk_f16_f32 v2, v2, v3
	v_cvt_pk_f16_f32 v3, v4, v5
	v_pk_add_f32 v[4:5], v[78:79], v[10:11]
	v_pk_add_f32 v[6:7], v[80:81], v[12:13]
	v_pk_mul_f32 v[4:5], v[202:203], v[4:5] op_sel_hi:[0,1]
	v_pk_mul_f32 v[6:7], v[202:203], v[6:7] op_sel_hi:[0,1]
	v_pk_add_f32 v[44:45], v[68:69], v[64:65]
	v_cvt_pk_f16_f32 v4, v4, v5
	v_cvt_pk_f16_f32 v5, v6, v7
	s_waitcnt vmcnt(0)
	v_pk_add_f32 v[6:7], v[34:35], v[30:31]
	v_pk_add_f32 v[8:9], v[36:37], v[32:33]
	v_pk_mul_f32 v[42:43], v[202:203], v[42:43] op_sel_hi:[0,1]
	v_pk_mul_f32 v[44:45], v[202:203], v[44:45] op_sel_hi:[0,1]
	v_pk_mul_f32 v[6:7], v[202:203], v[6:7] op_sel_hi:[0,1]
	v_pk_mul_f32 v[8:9], v[202:203], v[8:9] op_sel_hi:[0,1]
	v_cvt_pk_f16_f32 v42, v42, v43
	v_cvt_pk_f16_f32 v43, v44, v45
	v_cvt_pk_f16_f32 v6, v6, v7
	v_cvt_pk_f16_f32 v7, v8, v9
	ds_write2_b64 v155, v[38:39], v[42:43] offset0:20 offset1:22
	v_pk_add_f32 v[38:39], v[66:67], v[46:47]
	v_pk_add_f32 v[42:43], v[68:69], v[48:49]
	ds_write2_b64 v155, v[2:3], v[6:7] offset0:28 offset1:30
	v_pk_add_f32 v[2:3], v[34:35], v[14:15]
	v_pk_add_f32 v[6:7], v[36:37], v[16:17]
	v_pk_mul_f32 v[38:39], v[202:203], v[38:39] op_sel_hi:[0,1]
	v_pk_mul_f32 v[42:43], v[202:203], v[42:43] op_sel_hi:[0,1]
	v_pk_mul_f32 v[2:3], v[202:203], v[2:3] op_sel_hi:[0,1]
	v_pk_mul_f32 v[6:7], v[202:203], v[6:7] op_sel_hi:[0,1]
	v_cvt_pk_f16_f32 v38, v38, v39
	v_cvt_pk_f16_f32 v39, v42, v43
	v_cvt_pk_f16_f32 v2, v2, v3
	v_cvt_pk_f16_f32 v3, v6, v7
	ds_write2_b64 v176, v[40:41], v[38:39] offset0:84 offset1:86
	ds_write2_b64 v176, v[4:5], v[2:3] offset0:92 offset1:94
.Lepi_join:
	s_and_saveexec_b64 s[4:5], s[6:7]
	v_lshl_add_u32 v2, v0, 2, 0
	v_add_u32_e32 v2, 0x20800, v2
	v_mov_b32_e32 v3, 0
	ds_write_b32 v2, v3
	s_or_b64 exec, exec, s[4:5]
	s_waitcnt lgkmcnt(0)
	s_barrier
	s_mov_b64 s[4:5], -1
	s_and_b64 vcc, exec, s[22:23]
	s_cbranch_vccnz .LBB1_7
	s_andn2_b64 vcc, exec, s[4:5]
	s_cbranch_vccz .LBB1_14
